# stick-breaking attention: next tile's K and V loads issued right after the K / V LDS writes (one tile earlier), 2 VALU per load address instead of 6
# speedup vs baseline: 1.0060x; 1.0060x over previous
.LBB0_452:
	s_or_b64 exec, exec, s[10:11]
	v_readfirstlane_b32 s10, v0
	s_cmpk_gt_i32 s10, 0x7ff
	s_cselect_b64 s[30:31], -1, 0
	s_and_b64 vcc, exec, s[30:31]
	s_cbranch_vccnz .LBB0_447
	s_lshl_b32 s14, s10, 1
	s_and_b32 s47, s10, 0x780
	s_lshl_b32 s11, s10, 5
	s_add_i32 s10, s14, s46
	s_and_b32 s56, s11, 0xfe0
	s_and_b32 s57, s10, 0xfffff000
	s_or_b32 s15, s57, s56
	s_lshl_b32 s10, s47, 1
	s_add_u32 s10, s50, s10
	s_addc_u32 s11, s51, 0
	v_add_u32_e32 v32, s15, v174
	v_mov_b64_e32 v[24:25], s[10:11]
	v_add_u32_e32 v34, s15, v175
	v_add_u32_e32 v36, s15, v176
	v_add_u32_e32 v38, s15, v177
	v_add_u32_e32 v40, s15, v178
	v_add_u32_e32 v41, s15, v179
	v_mad_i64_i32 v[0:1], s[12:13], v32, s3, v[24:25]
	v_mad_i64_i32 v[2:3], s[12:13], v34, s3, v[24:25]
	v_mad_i64_i32 v[8:9], s[12:13], v36, s3, v[24:25]
	v_mad_i64_i32 v[10:11], s[12:13], v38, s3, v[24:25]
	v_mad_i64_i32 v[16:17], s[12:13], v40, s3, v[24:25]
	v_mad_i64_i32 v[18:19], s[12:13], v41, s3, v[24:25]
	v_lshl_add_u64 v[0:1], v[0:1], 0, v[160:161]
	v_lshl_add_u64 v[4:5], v[2:3], 0, v[160:161]
	v_lshl_add_u64 v[8:9], v[8:9], 0, v[160:161]
	v_lshl_add_u64 v[12:13], v[10:11], 0, v[160:161]
	v_lshl_add_u64 v[16:17], v[16:17], 0, v[160:161]
	v_lshl_add_u64 v[20:21], v[18:19], 0, v[160:161]
	global_load_dwordx4 v[0:3], v[0:1], off
	s_nop 0
	global_load_dwordx4 v[4:7], v[4:5], off
	s_nop 0
	global_load_dwordx4 v[8:11], v[8:9], off
	s_nop 0
	global_load_dwordx4 v[12:15], v[12:13], off
	s_nop 0
	global_load_dwordx4 v[16:19], v[16:17], off
	s_nop 0
	global_load_dwordx4 v[20:23], v[20:21], off
	v_mov_b32_e32 v147, v161
	v_lshl_add_u64 v[148:149], s[10:11], 0, v[146:147]
	s_mov_b64 s[100:101], 0x2000
	v_lshl_add_u64 v[216:217], v[148:149], 0, s[100:101]
	v_mad_i64_i32 v[32:33], s[10:11], v32, s3, v[148:149]
	v_add_co_u32_e32 v32, vcc, s93, v32
	v_mad_i64_i32 v[34:35], s[10:11], v34, s3, v[148:149]
	s_nop 0
	v_addc_co_u32_e32 v33, vcc, 0, v33, vcc
	v_add_co_u32_e32 v34, vcc, s93, v34
	v_mad_i64_i32 v[36:37], s[10:11], v36, s3, v[148:149]
	s_nop 0
	v_addc_co_u32_e32 v35, vcc, 0, v35, vcc
	v_add_u32_e32 v42, s15, v180
	v_add_u32_e32 v43, s15, v181
	v_add_co_u32_e32 v36, vcc, s93, v36
	v_mad_i64_i32 v[26:27], s[12:13], v42, s3, v[24:25]
	v_mad_i64_i32 v[24:25], s[12:13], v43, s3, v[24:25]
	v_mad_i64_i32 v[38:39], s[10:11], v38, s3, v[148:149]
	v_addc_co_u32_e32 v37, vcc, 0, v37, vcc
	v_lshl_add_u64 v[26:27], v[26:27], 0, v[160:161]
	v_lshl_add_u64 v[28:29], v[24:25], 0, v[160:161]
	v_add_co_u32_e32 v38, vcc, s93, v38
	global_load_dwordx4 v[24:27], v[26:27], off
	s_nop 0
	global_load_dwordx4 v[28:31], v[28:29], off
	v_addc_co_u32_e32 v39, vcc, 0, v39, vcc
	global_load_dwordx4 v[80:83], v[32:33], off offset:-4096
	global_load_dwordx4 v[84:87], v[32:33], off
	global_load_dwordx4 v[88:91], v[34:35], off offset:-4096
	global_load_dwordx4 v[92:95], v[34:35], off
	global_load_dwordx4 v[96:99], v[36:37], off offset:-4096
	global_load_dwordx4 v[100:103], v[36:37], off
	v_mov_b32_e32 v48, 0
	s_mov_b32 s58, 0
	v_mov_b32_e32 v205, 1.0
	v_mov_b32_e32 v49, v48
	v_mov_b32_e32 v50, v48
	v_mov_b32_e32 v51, v48
	v_mov_b32_e32 v52, v48
	v_mov_b32_e32 v53, v48
	v_mov_b32_e32 v54, v48
	v_mov_b32_e32 v55, v48
	v_mov_b32_e32 v56, v48
	v_mov_b32_e32 v57, v48
	v_mov_b32_e32 v58, v48
	v_mov_b32_e32 v59, v48
	v_mov_b32_e32 v60, v48
	s_waitcnt vmcnt(0)
	ds_write_b128 v190, v[0:3] offset:8192
	ds_write_b128 v191, v[4:7] offset:8192
	ds_write_b128 v192, v[8:11] offset:8192
	ds_write_b128 v193, v[12:15] offset:8192
	ds_write_b128 v194, v[16:19] offset:8192
	ds_write_b128 v195, v[20:23] offset:8192
	v_mad_i64_i32 v[0:1], s[10:11], v40, s3, v[148:149]
	v_add_co_u32_e32 v0, vcc, s93, v0
	global_load_dwordx4 v[104:107], v[38:39], off offset:-4096
	global_load_dwordx4 v[108:111], v[38:39], off
	v_addc_co_u32_e32 v1, vcc, 0, v1, vcc
	global_load_dwordx4 v[112:115], v[0:1], off offset:-4096
	global_load_dwordx4 v[116:119], v[0:1], off
	v_mad_i64_i32 v[0:1], s[10:11], v41, s3, v[148:149]
	v_add_co_u32_e32 v0, vcc, s93, v0
	v_mov_b32_e32 v61, v48
	s_nop 0
	v_addc_co_u32_e32 v1, vcc, 0, v1, vcc
	global_load_dwordx4 v[120:123], v[0:1], off offset:-4096
	global_load_dwordx4 v[124:127], v[0:1], off
	v_mad_i64_i32 v[0:1], s[10:11], v42, s3, v[148:149]
	v_add_co_u32_e32 v0, vcc, s93, v0
	v_mov_b32_e32 v62, v48
	s_nop 0
	v_addc_co_u32_e32 v1, vcc, 0, v1, vcc
	global_load_dwordx4 v[128:131], v[0:1], off offset:-4096
	global_load_dwordx4 v[132:135], v[0:1], off
	v_mad_i64_i32 v[0:1], s[10:11], v43, s3, v[148:149]
	v_add_co_u32_e32 v0, vcc, s93, v0
	s_add_i32 s10, s43, s14
	s_nop 0
	v_addc_co_u32_e32 v1, vcc, 0, v1, vcc
	global_load_dwordx4 v[136:139], v[0:1], off offset:-4096
	global_load_dwordx4 v[140:143], v[0:1], off
	s_and_b32 s10, s10, 0xfffff000
	s_or_b32 s10, s56, s10
	ds_write_b128 v196, v[24:27] offset:8192
	ds_write_b128 v197, v[28:31] offset:8192
	v_add_u32_e32 v147, s10, v182
	v_add_u32_e32 v198, s10, v183
	v_add_u32_e32 v199, s10, v184
	v_add_u32_e32 v200, s10, v185
	v_add_u32_e32 v201, s10, v186
	v_add_u32_e32 v202, s10, v187
	v_add_u32_e32 v203, s10, v188
	v_add_u32_e32 v204, s10, v189
	v_mov_b32_e32 v63, v48
	v_mov_b32_e32 v32, v48
	v_mov_b32_e32 v33, v48
	v_mov_b32_e32 v34, v48
	v_mov_b32_e32 v35, v48
	v_mov_b32_e32 v36, v48
	v_mov_b32_e32 v37, v48
	v_mov_b32_e32 v38, v48
	v_mov_b32_e32 v39, v48
	v_mov_b32_e32 v40, v48
	v_mov_b32_e32 v41, v48
	v_mov_b32_e32 v42, v48
	v_mov_b32_e32 v43, v48
	v_mov_b32_e32 v44, v48
	v_mov_b32_e32 v45, v48
	v_mov_b32_e32 v46, v48
	v_mov_b32_e32 v47, v48
	v_mov_b32_e32 v16, v48
	v_mov_b32_e32 v17, v48
	v_mov_b32_e32 v18, v48
	v_mov_b32_e32 v19, v48
	v_mov_b32_e32 v20, v48
	v_mov_b32_e32 v21, v48
	v_mov_b32_e32 v22, v48
	v_mov_b32_e32 v23, v48
	v_mov_b32_e32 v24, v48
	v_mov_b32_e32 v25, v48
	v_mov_b32_e32 v26, v48
	v_mov_b32_e32 v27, v48
	v_mov_b32_e32 v28, v48
	v_mov_b32_e32 v29, v48
	v_mov_b32_e32 v30, v48
	v_mov_b32_e32 v31, v48
	v_mov_b32_e32 v0, v48
	v_mov_b32_e32 v1, v48
	v_mov_b32_e32 v2, v48
	v_mov_b32_e32 v3, v48
	v_mov_b32_e32 v4, v48
	v_mov_b32_e32 v5, v48
	v_mov_b32_e32 v6, v48
	v_mov_b32_e32 v7, v48
	v_mov_b32_e32 v8, v48
	v_mov_b32_e32 v9, v48
	v_mov_b32_e32 v10, v48
	v_mov_b32_e32 v11, v48
	v_mov_b32_e32 v12, v48
	v_mov_b32_e32 v13, v48
	v_mov_b32_e32 v14, v48
	v_mov_b32_e32 v15, v48
	s_branch .LBB0_455

.LBB0_455:
	v_mov_b32_e32 v206, v172
	s_cmp_lg_u32 s58, 0
	v_lshrrev_b32_e32 v64, 4, v206
	v_lshlrev_b32_e32 v66, 4, v206
	v_lshlrev_b32_e32 v65, 8, v64
	v_lshlrev_b32_e32 v64, 6, v64
	v_and_b32_e32 v66, 0xf0, v66
	v_xad_u32 v64, v64, v66, v65
	v_lshlrev_b32_e32 v65, 2, v206
	v_and_b32_e32 v168, 31, v206
	v_ashrrev_i32_e32 v169, 5, v206
	v_and_b32_e32 v65, 12, v65
	v_bfe_u32 v207, v206, 2, 2
	v_bitop3_b32 v65, v65, v169, v207 bitop3:0x36
	v_add_u32_e32 v158, s42, v64
	v_xad_u32 v159, v64, 16, s42
	v_xad_u32 v162, v64, 32, s42
	v_xad_u32 v163, v64, 48, s42
	v_lshlrev_b32_e32 v64, 8, v168
	v_lshl_add_u32 v166, v65, 4, v64
	s_waitcnt vmcnt(15)
	ds_write_b128 v158, v[80:83]
	s_waitcnt vmcnt(13)
	ds_write_b128 v159, v[88:91] offset:1024
	s_waitcnt vmcnt(11)
	ds_write_b128 v162, v[96:99] offset:2048
	s_waitcnt vmcnt(9)
	ds_write_b128 v163, v[104:107] offset:3072
	s_waitcnt vmcnt(7)
	ds_write_b128 v158, v[112:115] offset:4096
	s_waitcnt vmcnt(5)
	ds_write_b128 v159, v[120:123] offset:5120
	s_waitcnt vmcnt(3)
	ds_write_b128 v162, v[128:131] offset:6144
	s_waitcnt vmcnt(1)
	ds_write_b128 v163, v[136:139] offset:7168
	v_add_u32_e32 v218, s58, v204
	v_mad_i64_i32 v[80:81], s[100:101], v218, s3, v[216:217]
	global_load_dwordx4 v[80:83], v[80:81], off offset:-4096
	v_add_u32_e32 v218, s58, v203
	v_mad_i64_i32 v[88:89], s[100:101], v218, s3, v[216:217]
	global_load_dwordx4 v[88:91], v[88:89], off offset:-4096
	v_add_u32_e32 v218, s58, v202
	v_mad_i64_i32 v[96:97], s[100:101], v218, s3, v[216:217]
	global_load_dwordx4 v[96:99], v[96:97], off offset:-4096
	v_add_u32_e32 v218, s58, v201
	v_mad_i64_i32 v[104:105], s[100:101], v218, s3, v[216:217]
	global_load_dwordx4 v[104:107], v[104:105], off offset:-4096
	v_add_u32_e32 v218, s58, v200
	v_mad_i64_i32 v[112:113], s[100:101], v218, s3, v[216:217]
	global_load_dwordx4 v[112:115], v[112:113], off offset:-4096
	v_add_u32_e32 v218, s58, v199
	v_mad_i64_i32 v[120:121], s[100:101], v218, s3, v[216:217]
	global_load_dwordx4 v[120:123], v[120:121], off offset:-4096
	v_add_u32_e32 v218, s58, v198
	v_mad_i64_i32 v[128:129], s[100:101], v218, s3, v[216:217]
	global_load_dwordx4 v[128:131], v[128:129], off offset:-4096
	v_add_u32_e32 v218, s58, v147
	v_mad_i64_i32 v[136:137], s[100:101], v218, s3, v[216:217]
	global_load_dwordx4 v[136:139], v[136:137], off offset:-4096
	v_add_u32_e32 v68, s42, v166
	ds_read_b128 v[64:67], v68
	ds_read_b128 v[68:71], v68 offset:8192
	s_waitcnt lgkmcnt(0)
	v_mfma_f32_32x32x16_bf16 v[64:79], v[64:67], v[68:71], 0
	v_xad_u32 v154, v166, 32, s42
	ds_read_b128 v[150:153], v154
	ds_read_b128 v[154:157], v154 offset:8192
	v_xad_u32 v167, v166, 64, s42
	s_waitcnt lgkmcnt(0)
	v_mfma_f32_32x32x16_bf16 v[64:79], v[150:153], v[154:157], v[64:79]
	ds_read_b128 v[150:153], v167
	ds_read_b128 v[154:157], v167 offset:8192
	v_xor_b32_e32 v167, 0x60, v166
	v_add_u32_e32 v167, s42, v167
	s_waitcnt lgkmcnt(0)
	v_mfma_f32_32x32x16_bf16 v[64:79], v[150:153], v[154:157], v[64:79]
	ds_read_b128 v[150:153], v167
	ds_read_b128 v[154:157], v167 offset:8192
	v_xor_b32_e32 v167, 0x80, v166
	v_add_u32_e32 v167, s42, v167
	s_waitcnt lgkmcnt(0)
	v_mfma_f32_32x32x16_bf16 v[64:79], v[150:153], v[154:157], v[64:79]
	ds_read_b128 v[150:153], v167
	ds_read_b128 v[154:157], v167 offset:8192
	v_xor_b32_e32 v167, 0xa0, v166
	v_add_u32_e32 v167, s42, v167
	s_waitcnt lgkmcnt(0)
	v_mfma_f32_32x32x16_bf16 v[64:79], v[150:153], v[154:157], v[64:79]
	ds_read_b128 v[150:153], v167
	ds_read_b128 v[154:157], v167 offset:8192
	v_xor_b32_e32 v167, 0xc0, v166
	v_add_u32_e32 v167, s42, v167
	ds_read_b128 v[208:211], v167
	s_waitcnt lgkmcnt(1)
	v_mfma_f32_32x32x16_bf16 v[64:79], v[150:153], v[154:157], v[64:79]
	ds_read_b128 v[150:153], v167 offset:8192
	v_xor_b32_e32 v154, 0xe0, v166
	v_add_u32_e32 v166, s42, v154
	ds_read_b128 v[154:157], v166
	ds_read_b128 v[212:215], v166 offset:8192
	s_waitcnt lgkmcnt(0)
	ds_write_b128 v158, v[84:87]
	ds_write_b128 v159, v[92:95] offset:1024
	ds_write_b128 v162, v[100:103] offset:2048
	ds_write_b128 v163, v[108:111] offset:3072
	ds_write_b128 v158, v[116:119] offset:4096
	ds_write_b128 v159, v[124:127] offset:5120
	ds_write_b128 v162, v[132:135] offset:6144
	s_waitcnt vmcnt(8)
	ds_write_b128 v163, v[140:143] offset:7168
	v_add_u32_e32 v218, s58, v204
	v_mad_i64_i32 v[84:85], s[100:101], v218, s3, v[216:217]
	global_load_dwordx4 v[84:87], v[84:85], off
	v_add_u32_e32 v218, s58, v203
	v_mad_i64_i32 v[92:93], s[100:101], v218, s3, v[216:217]
	global_load_dwordx4 v[92:95], v[92:93], off
	v_add_u32_e32 v218, s58, v202
	v_mad_i64_i32 v[100:101], s[100:101], v218, s3, v[216:217]
	global_load_dwordx4 v[100:103], v[100:101], off
	v_add_u32_e32 v218, s58, v201
	v_mad_i64_i32 v[108:109], s[100:101], v218, s3, v[216:217]
	global_load_dwordx4 v[108:111], v[108:109], off
	v_add_u32_e32 v218, s58, v200
	v_mad_i64_i32 v[116:117], s[100:101], v218, s3, v[216:217]
	global_load_dwordx4 v[116:119], v[116:117], off
	v_add_u32_e32 v218, s58, v199
	v_mad_i64_i32 v[124:125], s[100:101], v218, s3, v[216:217]
	global_load_dwordx4 v[124:127], v[124:125], off
	v_add_u32_e32 v218, s58, v198
	v_mad_i64_i32 v[132:133], s[100:101], v218, s3, v[216:217]
	global_load_dwordx4 v[132:135], v[132:133], off
	v_add_u32_e32 v218, s58, v147
	v_mad_i64_i32 v[140:141], s[100:101], v218, s3, v[216:217]
	global_load_dwordx4 v[140:143], v[140:141], off
	s_waitcnt lgkmcnt(10)
	v_mfma_f32_32x32x16_bf16 v[64:79], v[208:211], v[150:153], v[64:79]
	s_waitcnt lgkmcnt(8)
	v_mfma_f32_32x32x16_bf16 v[64:79], v[154:157], v[212:215], v[64:79]
	s_nop 11
	v_mul_f32_e32 v64, 0x3db504f3, v64
	v_mul_f32_e32 v65, 0x3db504f3, v65
	v_min_f32_e32 v64, 0x42a00000, v64
	v_min_f32_e32 v65, 0x42a00000, v65
	v_mul_f32_e32 v67, 0x3db504f3, v67
	v_mul_f32_e32 v64, 0x3fb8aa3b, v64
	v_mul_f32_e32 v65, 0x3fb8aa3b, v65
	v_min_f32_e32 v67, 0x42a00000, v67
	v_exp_f32_e32 v64, v64
	v_exp_f32_e32 v65, v65
	v_mul_f32_e32 v67, 0x3fb8aa3b, v67
	v_exp_f32_e32 v152, v67
	v_mul_f32_e32 v67, 0x3db504f3, v68
	v_min_f32_e32 v67, 0x42a00000, v67
	v_mul_f32_e32 v67, 0x3fb8aa3b, v67
	v_add_f32_e32 v150, 1.0, v64
	v_add_f32_e32 v151, 1.0, v65
	v_exp_f32_e32 v68, v67
	v_mul_f32_e32 v67, 0x3db504f3, v69
	v_rcp_f32_e32 v154, v150
	v_rcp_f32_e32 v155, v151
	v_min_f32_e32 v67, 0x42a00000, v67
	v_mul_f32_e32 v67, 0x3fb8aa3b, v67
	v_exp_f32_e32 v69, v67
	v_pk_mul_f32 v[150:151], v[64:65], v[154:155]
	v_add_f32_e32 v65, 1.0, v152
	v_rcp_f32_e32 v67, v65
	v_add_f32_e32 v65, 1.0, v68
	v_rcp_f32_e32 v156, v65
	v_add_f32_e32 v65, 1.0, v69
	v_mul_f32_e32 v66, 0x3db504f3, v66
	v_rcp_f32_e32 v157, v65
	v_min_f32_e32 v66, 0x42a00000, v66
	v_mul_f32_e32 v66, 0x3fb8aa3b, v66
	v_exp_f32_e32 v66, v66
	v_mul_f32_e32 v210, v152, v67
	v_pk_mul_f32 v[152:153], v[68:69], v[156:157]
	v_mul_f32_e32 v68, 0x3db504f3, v71
	v_mul_f32_e32 v65, 0x3db504f3, v70
	v_min_f32_e32 v68, 0x42a00000, v68
	v_min_f32_e32 v65, 0x42a00000, v65
	v_mul_f32_e32 v68, 0x3fb8aa3b, v68
	v_add_f32_e32 v64, 1.0, v66
	v_mul_f32_e32 v65, 0x3fb8aa3b, v65
	v_exp_f32_e32 v162, v68
	v_mul_f32_e32 v68, 0x3db504f3, v72
	v_rcp_f32_e32 v64, v64
	v_exp_f32_e32 v65, v65
	v_min_f32_e32 v68, 0x42a00000, v68
	v_mul_f32_e32 v68, 0x3fb8aa3b, v68
	v_exp_f32_e32 v70, v68
	v_mul_f32_e32 v68, 0x3db504f3, v73
	v_min_f32_e32 v68, 0x42a00000, v68
	v_mul_f32_e32 v211, v66, v64
	v_add_f32_e32 v66, 1.0, v65
	v_mul_f32_e32 v68, 0x3fb8aa3b, v68
	v_rcp_f32_e32 v66, v66
	v_exp_f32_e32 v71, v68
	v_mul_f32_e32 v68, 0x3db504f3, v74
	v_min_f32_e32 v68, 0x42a00000, v68
	v_mul_f32_e32 v68, 0x3fb8aa3b, v68
	v_exp_f32_e32 v72, v68
	v_mul_f32_e32 v212, v65, v66
	v_add_f32_e32 v65, 1.0, v162
	v_rcp_f32_e32 v69, v65
	v_add_f32_e32 v65, 1.0, v70
	v_rcp_f32_e32 v158, v65
	v_add_f32_e32 v65, 1.0, v71
	v_rcp_f32_e32 v159, v65
	v_add_f32_e32 v65, 1.0, v72
	v_rcp_f32_e32 v68, v65
	v_mul_f32_e32 v65, 0x3db504f3, v75
	v_min_f32_e32 v65, 0x42a00000, v65
	v_mul_f32_e32 v65, 0x3fb8aa3b, v65
	v_exp_f32_e32 v65, v65
	v_pk_mul_f32 v[74:75], v[70:71], v[158:159]
	v_mul_f32_e32 v213, v72, v68
	v_mul_f32_e32 v214, v162, v69
	v_add_f32_e32 v70, 1.0, v65
	v_rcp_f32_e32 v71, v70
	v_mul_f32_e32 v70, 0x3db504f3, v76
	v_min_f32_e32 v70, 0x42a00000, v70
	v_mul_f32_e32 v70, 0x3fb8aa3b, v70
	v_exp_f32_e32 v72, v70
	v_mul_f32_e32 v70, 0x3db504f3, v77
	v_min_f32_e32 v70, 0x42a00000, v70
	v_mul_f32_e32 v70, 0x3fb8aa3b, v70
	v_exp_f32_e32 v73, v70
	v_mul_f32_e32 v70, 0x3db504f3, v78
	v_min_f32_e32 v70, 0x42a00000, v70
	v_mul_f32_e32 v70, 0x3fb8aa3b, v70
	v_exp_f32_e32 v76, v70
	v_mul_f32_e32 v70, 0x3db504f3, v79
	v_min_f32_e32 v70, 0x42a00000, v70
	v_mul_f32_e32 v70, 0x3fb8aa3b, v70
	v_exp_f32_e32 v77, v70
	v_mul_f32_e32 v215, v65, v71
	v_add_f32_e32 v65, 1.0, v72
	v_rcp_f32_e32 v166, v65
	v_add_f32_e32 v65, 1.0, v73
	v_rcp_f32_e32 v167, v65
	v_add_f32_e32 v65, 1.0, v76
	v_rcp_f32_e32 v70, v65
	v_add_f32_e32 v65, 1.0, v77
	v_rcp_f32_e32 v65, v65
	v_pk_mul_f32 v[72:73], v[72:73], v[166:167]
	v_mul_f32_e32 v208, v76, v70
	v_mul_f32_e32 v209, v77, v65
	s_cbranch_scc1 .LBB0_457
	v_lshlrev_b32_e32 v76, 2, v169
	v_or_b32_e32 v77, 1, v76
	v_cmp_lt_i32_e32 vcc, v76, v168
	v_cmp_lt_i32_e64 s[10:11], v77, v168
	v_or_b32_e32 v77, 2, v76
	v_cndmask_b32_e32 v150, 0, v150, vcc
	s_or_b64 s[70:71], s[10:11], vcc
	v_cmp_lt_i32_e32 vcc, v77, v168
	v_or_b32_e32 v77, 3, v76
	v_cmp_lt_i32_e64 s[12:13], v77, v168
	v_add_u32_e32 v77, 8, v76
	v_cmp_lt_i32_e64 s[14:15], v77, v168
	v_add_u32_e32 v77, 10, v76
	v_add_u32_e32 v78, 9, v76
	v_cmp_lt_i32_e64 s[16:17], v77, v168
	v_add_u32_e32 v77, 11, v76
	v_cndmask_b32_e32 v211, 0, v211, vcc
	s_or_b64 s[72:73], s[12:13], vcc
	v_cmp_lt_i32_e32 vcc, v78, v168
	v_cmp_lt_i32_e64 s[18:19], v77, v168
	s_or_b64 s[20:21], vcc, s[14:15]
	v_cndmask_b32_e64 v212, 0, v212, s[16:17]
	s_or_b64 s[16:17], s[18:19], s[16:17]
	s_or_b64 s[20:21], s[20:21], s[16:17]
	v_cndmask_b32_e64 v156, 1.0, v156, s[20:21]
	s_or_b64 s[20:21], s[20:21], s[72:73]
	v_cndmask_b32_e64 v151, 0, v151, s[10:11]
	s_or_b64 s[10:11], s[20:21], s[10:11]
	v_cndmask_b32_e32 v153, 0, v153, vcc
	v_cndmask_b32_e64 v155, 1.0, v155, s[10:11]
	s_or_b64 s[10:11], s[20:21], s[70:71]
	s_or_b64 vcc, s[16:17], vcc
	v_cndmask_b32_e64 v154, 1.0, v154, s[10:11]
	s_or_b64 s[10:11], vcc, s[14:15]
	v_add_u32_e32 v77, 16, v76
	v_cndmask_b32_e32 v157, 1.0, v157, vcc
	s_or_b64 vcc, s[10:11], s[12:13]
	v_cmp_lt_i32_e64 s[10:11], v77, v168
	v_add_u32_e32 v77, 18, v76
	v_cndmask_b32_e64 v210, 0, v210, s[12:13]
	v_cmp_lt_i32_e64 s[12:13], v77, v168
	v_add_u32_e32 v77, 19, v76
	v_cndmask_b32_e64 v152, 0, v152, s[14:15]
	v_add_u32_e32 v78, 17, v76
	v_cmp_lt_i32_e64 s[14:15], v77, v168
	v_cndmask_b32_e32 v67, 1.0, v67, vcc
	v_cmp_lt_i32_e32 vcc, v78, v168
	v_cndmask_b32_e64 v213, 0, v213, s[12:13]
	s_or_b64 s[12:13], s[14:15], s[12:13]
	v_cndmask_b32_e32 v75, 0, v75, vcc
	s_or_b64 vcc, s[12:13], vcc
	v_add_u32_e32 v77, 24, v76
	v_cndmask_b32_e64 v74, 0, v74, s[10:11]
	v_cndmask_b32_e32 v159, 1.0, v159, vcc
	s_or_b64 vcc, vcc, s[10:11]
	v_add_u32_e32 v78, 25, v76
	v_cmp_lt_i32_e64 s[10:11], v77, v168
	v_add_u32_e32 v77, 26, v76
	v_add_u32_e32 v76, 27, v76
	v_cndmask_b32_e64 v215, 0, v215, s[14:15]
	v_cndmask_b32_e64 v68, 1.0, v68, s[12:13]
	v_cndmask_b32_e64 v71, 1.0, v71, s[14:15]
	v_cmp_lt_i32_e64 s[12:13], v77, v168
	v_cmp_lt_i32_e64 s[14:15], v76, v168
	v_cndmask_b32_e32 v158, 1.0, v158, vcc
	v_cmp_lt_i32_e32 vcc, v78, v168
	v_cndmask_b32_e64 v208, 0, v208, s[12:13]
	s_or_b64 s[12:13], s[14:15], s[12:13]
	v_cndmask_b32_e32 v73, 0, v73, vcc
	s_or_b64 vcc, s[12:13], vcc
	v_cndmask_b32_e32 v167, 1.0, v167, vcc
	s_or_b64 vcc, vcc, s[10:11]
	v_cndmask_b32_e64 v214, 0, v214, s[18:19]
	v_cndmask_b32_e64 v66, 1.0, v66, s[16:17]
	v_cndmask_b32_e64 v64, 1.0, v64, s[20:21]
	v_cndmask_b32_e64 v69, 1.0, v69, s[18:19]
	v_cndmask_b32_e64 v72, 0, v72, s[10:11]
	v_cndmask_b32_e64 v209, 0, v209, s[14:15]
	v_cndmask_b32_e64 v70, 1.0, v70, s[12:13]
	v_cndmask_b32_e32 v166, 1.0, v166, vcc
	v_cndmask_b32_e64 v65, 1.0, v65, s[14:15]
.LBB0_457:
	v_mov_b32_e32 v76, v71
	v_mov_b32_e32 v77, v65
	v_mov_b32_e32 v78, v68
	v_mov_b32_e32 v79, v70
	v_pk_mul_f32 v[76:77], v[76:77], v[78:79]
	v_mov_b32_e32 v78, v159
	v_mov_b32_e32 v79, v167
	v_pk_mul_f32 v[78:79], v[78:79], v[76:77]
	v_mov_b32_e32 v159, v166
	v_pk_mul_f32 v[166:167], v[158:159], v[78:79]
	v_and_b32_e32 v162, 32, v206
	v_mov_b32_e32 v68, v167
	v_mov_b32_e32 v70, v167
	v_mov_b32_e32 v158, v166
	v_mov_b32_e32 v163, v166
	v_permlane32_swap_b32_e32 v68, v70
	s_nop 0
	v_permlane32_swap_b32_e32 v158, v163
	v_cmp_eq_u32_e64 s[10:11], 0, v162
	v_mul_f32_e32 v66, v69, v66
	s_add_i32 s12, s56, s58
	v_cndmask_b32_e64 v159, v68, v70, s[10:11]
	v_cndmask_b32_e64 v158, v158, v163, s[10:11]
	v_pk_mul_f32 v[168:169], v[166:167], v[158:159]
	v_mul_f32_e32 v166, v157, v66
	v_mov_b32_e32 v157, v168
	v_mov_b32_e32 v167, v169
	v_pk_mul_f32 v[170:171], v[156:157], v[166:167]
	v_mul_f32_e32 v157, v67, v64
	v_mul_f32_e32 v156, v155, v157
	v_mul_f32_e32 v64, v154, v156
	v_mov_b32_e32 v68, v170
	v_mov_b32_e32 v70, v170
	v_mov_b32_e32 v154, v64
	v_mov_b32_e32 v155, v64
	v_permlane32_swap_b32_e32 v68, v70
	s_cmp_eq_u32 s12, 0
	v_permlane32_swap_b32_e32 v154, v155
	s_branch .LBB0_454

.LBB0_804:
	v_mov_b32_e32 v89, v90
	s_add_i32 s15, s16, s28
	s_and_b32 s17, s14, 1
	s_waitcnt lgkmcnt(0)
	s_barrier
	v_add_u32_e32 v0, v101, v92
	s_cmpk_gt_i32 s15, 0x7fff
	v_lshlrev_b32_e32 v88, 4, v89
	s_waitcnt vmcnt(33)
	ds_write_b128 v0, v[16:19]
	s_waitcnt vmcnt(32)
	ds_write_b128 v104, v[20:23] offset:512
	s_waitcnt vmcnt(31)
	ds_write_b128 v105, v[24:27] offset:1024
	s_waitcnt vmcnt(30)
	ds_write_b128 v106, v[28:31] offset:1536
	s_waitcnt vmcnt(29)
	ds_write_b128 v107, v[32:35] offset:2048
	s_waitcnt vmcnt(28)
	ds_write_b128 v108, v[36:39] offset:2560
	s_waitcnt vmcnt(27)
	ds_write_b128 v109, v[40:43] offset:3072
	s_waitcnt vmcnt(26)
	ds_write_b128 v110, v[44:47] offset:3584
	s_waitcnt vmcnt(25)
	ds_write_b128 v0, v[48:51] offset:4096
	s_waitcnt vmcnt(24)
	ds_write_b128 v104, v[52:55] offset:4608
	s_waitcnt vmcnt(23)
	ds_write_b128 v105, v[56:59] offset:5120
	s_waitcnt vmcnt(22)
	ds_write_b128 v106, v[60:63] offset:5632
	s_waitcnt vmcnt(21)
	ds_write_b128 v107, v[64:67] offset:6144
	s_waitcnt vmcnt(20)
	ds_write_b128 v108, v[68:71] offset:6656
	s_waitcnt vmcnt(19)
	ds_write_b128 v109, v[72:75] offset:7168
	s_waitcnt vmcnt(18)
	ds_write_b128 v110, v[76:79] offset:7680
	s_waitcnt vmcnt(0)
	ds_write_b128 v111, v[84:87]
	ds_write_b128 v111, v[80:83] offset:128
	s_cselect_b64 s[6:7], -1, 0
	s_cmp_lt_i32 s15, 0x8000
	v_add_u32_e32 v0, 0, v88
	s_waitcnt lgkmcnt(0)
	s_barrier
	s_cselect_b32 s8, s15, s16
	v_add_u32_e32 v77, 0x20000, v0
	v_add_u32_e32 v0, v102, v93
	s_ashr_i32 s9, s8, 31
	ds_read_b128 v[0:3], v0
	ds_read_b128 v[4:7], v77
	s_lshr_b32 s10, s9, 20
	s_add_i32 s10, s8, s10
	s_ashr_i32 s10, s10, 12
	s_ashr_i32 s11, s10, 31
	s_lshl_b64 s[12:13], s[10:11], 21
	v_readlane_b32 s11, v253, 2
	v_and_b32_e32 v130, 31, v89
	s_waitcnt lgkmcnt(0)
	v_mfma_f32_32x32x16_bf16 v[0:15], v[0:3], v[4:7], 0
	s_add_u32 s12, s11, s12
	v_readlane_b32 s11, v253, 3
	v_lshlrev_b32_e32 v76, 4, v130
	s_addc_u32 s13, s11, s13
	v_lshl_or_b32 v16, v121, 9, v76
	v_add_u32_e32 v20, v102, v94
	global_load_dwordx4 v[16:19], v16, s[12:13]
	ds_read_b128 v[20:23], v20
	ds_read_b128 v[24:27], v77 offset:1024
	s_waitcnt lgkmcnt(0)
	v_mfma_f32_32x32x16_bf16 v[0:15], v[20:23], v[24:27], v[0:15]
	v_lshl_or_b32 v20, v123, 9, v76
	v_add_u32_e32 v24, v102, v95
	global_load_dwordx4 v[20:23], v20, s[12:13]
	ds_read_b128 v[24:27], v24
	ds_read_b128 v[28:31], v77 offset:2048
	v_add_u32_e32 v78, v103, v100
	v_add_u32_e32 v80, s44, v89
	s_movk_i32 s11, 0x100
	s_waitcnt lgkmcnt(0)
	v_mfma_f32_32x32x16_bf16 v[0:15], v[24:27], v[28:31], v[0:15]
	v_lshl_or_b32 v24, v116, 9, v76
	v_add_u32_e32 v28, v102, v96
	global_load_dwordx4 v[24:27], v24, s[12:13]
	ds_read_b128 v[28:31], v28
	ds_read_b128 v[32:35], v77 offset:3072
	v_cmp_gt_i32_e32 vcc, s11, v80
	s_waitcnt lgkmcnt(0)
	v_mfma_f32_32x32x16_bf16 v[0:15], v[28:31], v[32:35], v[0:15]
	v_lshl_or_b32 v28, v124, 9, v76
	v_add_u32_e32 v32, v102, v97
	global_load_dwordx4 v[28:31], v28, s[12:13]
	ds_read_b128 v[32:35], v32
	ds_read_b128 v[36:39], v77 offset:4096
	s_waitcnt lgkmcnt(0)
	v_mfma_f32_32x32x16_bf16 v[0:15], v[32:35], v[36:39], v[0:15]
	v_lshl_or_b32 v32, v119, 9, v76
	v_add_u32_e32 v36, v102, v98
	global_load_dwordx4 v[32:35], v32, s[12:13]
	ds_read_b128 v[36:39], v36
	ds_read_b128 v[40:43], v77 offset:5120
	s_waitcnt lgkmcnt(0)
	v_mfma_f32_32x32x16_bf16 v[0:15], v[36:39], v[40:43], v[0:15]
	v_lshl_or_b32 v36, v120, 9, v76
	v_add_u32_e32 v40, v102, v99
	global_load_dwordx4 v[36:39], v36, s[12:13]
	ds_read_b128 v[40:43], v40
	ds_read_b128 v[44:47], v77 offset:6144
	s_waitcnt lgkmcnt(0)
	v_mfma_f32_32x32x16_bf16 v[0:15], v[40:43], v[44:47], v[0:15]
	v_lshl_or_b32 v40, v117, 9, v76
	v_add_u32_e32 v44, v102, v100
	global_load_dwordx4 v[40:43], v40, s[12:13]
	ds_read_b128 v[44:47], v44
	ds_read_b128 v[48:51], v77 offset:7168
	s_waitcnt lgkmcnt(0)
	v_mfma_f32_32x32x16_bf16 v[0:15], v[44:47], v[48:51], v[0:15]
	v_lshl_or_b32 v44, v125, 9, v76
	v_add_u32_e32 v48, v103, v93
	global_load_dwordx4 v[44:47], v44, s[12:13]
	ds_read_b128 v[48:51], v48
	ds_read_b128 v[52:55], v77 offset:8192
	s_waitcnt lgkmcnt(0)
	v_mfma_f32_32x32x16_bf16 v[0:15], v[48:51], v[52:55], v[0:15]
	v_lshl_or_b32 v48, v118, 9, v76
	v_add_u32_e32 v52, v103, v94
	global_load_dwordx4 v[48:51], v48, s[12:13]
	ds_read_b128 v[52:55], v52
	ds_read_b128 v[56:59], v77 offset:9216
	s_waitcnt lgkmcnt(0)
	v_mfma_f32_32x32x16_bf16 v[0:15], v[52:55], v[56:59], v[0:15]
	v_lshl_or_b32 v52, v114, 9, v76
	v_add_u32_e32 v56, v103, v95
	global_load_dwordx4 v[52:55], v52, s[12:13]
	ds_read_b128 v[56:59], v56
	ds_read_b128 v[60:63], v77 offset:10240
	s_waitcnt lgkmcnt(0)
	v_mfma_f32_32x32x16_bf16 v[0:15], v[56:59], v[60:63], v[0:15]
	v_lshl_or_b32 v56, v115, 9, v76
	v_add_u32_e32 v60, v103, v96
	global_load_dwordx4 v[56:59], v56, s[12:13]
	ds_read_b128 v[60:63], v60
	ds_read_b128 v[64:67], v77 offset:11264
	s_waitcnt lgkmcnt(0)
	v_mfma_f32_32x32x16_bf16 v[0:15], v[60:63], v[64:67], v[0:15]
	v_lshl_or_b32 v60, v122, 9, v76
	v_add_u32_e32 v64, v103, v97
	global_load_dwordx4 v[60:63], v60, s[12:13]
	ds_read_b128 v[64:67], v64
	ds_read_b128 v[68:71], v77 offset:12288
	s_waitcnt lgkmcnt(0)
	v_mfma_f32_32x32x16_bf16 v[0:15], v[64:67], v[68:71], v[0:15]
	v_lshl_or_b32 v64, v126, 9, v76
	v_add_u32_e32 v68, v103, v98
	global_load_dwordx4 v[64:67], v64, s[12:13]
	ds_read_b128 v[68:71], v68
	ds_read_b128 v[72:75], v77 offset:13312
	s_waitcnt lgkmcnt(0)
	v_mfma_f32_32x32x16_bf16 v[0:15], v[68:71], v[72:75], v[0:15]
	v_lshl_or_b32 v68, v127, 9, v76
	v_add_u32_e32 v72, v103, v99
	global_load_dwordx4 v[68:71], v68, s[12:13]
	ds_read_b128 v[72:75], v72
	ds_read_b128 v[82:85], v77 offset:14336
	s_waitcnt lgkmcnt(0)
	v_mfma_f32_32x32x16_bf16 v[0:15], v[72:75], v[82:85], v[0:15]
	v_lshl_or_b32 v72, v128, 9, v76
	v_lshl_or_b32 v76, v129, 9, v76
	global_load_dwordx4 v[72:75], v72, s[12:13]
	ds_read_b128 v[82:85], v78
	ds_read_b128 v[114:117], v77 offset:15360
	global_load_dwordx4 v[76:79], v76, s[12:13]
	s_waitcnt lgkmcnt(0)
	v_mfma_f32_32x32x16_bf16 v[0:15], v[82:85], v[114:117], v[0:15]
	s_and_saveexec_b64 s[12:13], vcc
	s_cbranch_execz .LBB0_808
	s_lshl_b32 s10, s10, 12
	s_sub_i32 s18, s8, s10
	v_cmp_ge_i32_e32 vcc, s18, v80
	v_mov_b32_e32 v81, 0x1000
	s_and_saveexec_b64 s[10:11], vcc
	s_cbranch_execz .LBB0_807
	v_sub_u32_e32 v81, s18, v91
	v_mov_b32_e32 v82, 0x7f
	v_med3_i32 v81, v81, 0, v82
	v_add_u32_e32 v81, 0, v81
	v_add_u32_e32 v81, 0x25e80, v81
	ds_read_u8 v81, v81
	s_waitcnt lgkmcnt(0)
	v_lshlrev_b32_e32 v81, 7, v81

.LBB0_808:
	s_or_b64 exec, exec, s[12:13]
	v_readlane_b32 s10, v253, 24
	v_readlane_b32 s11, v253, 14
	s_add_i32 s10, s10, s16
	s_lshl_b64 s[8:9], s[8:9], 14
	v_and_or_b32 v80, v89, 7, s11
	v_lshrrev_b32_e32 v81, 3, v89
	v_readlane_b32 s11, v253, 18
	s_add_u32 s8, s50, s8
	s_addc_u32 s9, s51, s9
	v_add_lshl_u32 v81, v81, s11, 4
	v_lshl_add_u32 v80, v80, 9, v81
	global_load_dwordx4 v[84:87], v80, s[8:9]
	v_add_u32_e32 v80, 0x1000, v80
	v_ashrrev_i32_e32 v114, 3, v89
	global_load_dwordx4 v[80:83], v80, s[8:9]
	s_lshl_b32 s8, s17, 10
	v_readlane_b32 s9, v253, 15
	v_lshlrev_b32_e32 v114, 2, v114
	s_add_i32 s8, s9, s8
	v_and_b32_e32 v114, -16, v114
	v_add_u32_e32 v122, s8, v114
	ds_read_b128 v[114:117], v122
	ds_read_b128 v[118:121], v122 offset:32
	s_add_i32 s8, 0, 0x24a00
	v_lshl_add_u32 v123, v130, 2, s8
	s_mov_b32 s8, 0xff800000
	s_waitcnt lgkmcnt(1)
	v_add_u32_e32 v124, v123, v114
	v_add_u32_e32 v125, v123, v115
	v_add_u32_e32 v126, v123, v116
	v_add_u32_e32 v127, v123, v117
	ds_read_b128 v[114:117], v122 offset:64
	s_waitcnt lgkmcnt(1)
	v_add_u32_e32 v118, v123, v118
	v_add_u32_e32 v119, v123, v119
	v_add_u32_e32 v120, v123, v120
	v_add_u32_e32 v121, v123, v121
	s_waitcnt lgkmcnt(0)
	v_add_u32_e32 v128, v123, v114
	v_add_u32_e32 v129, v123, v115
	v_add_u32_e32 v131, v123, v116
	v_add_u32_e32 v132, v123, v117
	ds_read_b128 v[114:117], v122 offset:96
	v_readlane_b32 s9, v255, 14
	s_cmp_lt_i32 s10, 0x8000
	s_waitcnt lgkmcnt(0)
	v_add_u32_e32 v114, v123, v114
	v_add_u32_e32 v115, v123, v115
	v_add_u32_e32 v116, v123, v116
	v_add_u32_e32 v117, v123, v117
	ds_read_b32 v117, v117
	ds_read_b32 v116, v116
	ds_read_b32 v115, v115
	ds_read_b32 v114, v114
	ds_read_b32 v122, v132
	ds_read_b32 v123, v131
	ds_read_b32 v129, v129
	ds_read_b32 v128, v128
	ds_read_b32 v121, v121
	ds_read_b32 v120, v120
	ds_read_b32 v119, v119
	ds_read_b32 v118, v118
	ds_read_b32 v127, v127
	ds_read_b32 v126, v126
	ds_read_b32 v125, v125
	ds_read_b32 v124, v124
	s_waitcnt lgkmcnt(0)
	s_waitcnt lgkmcnt(0)
	s_nop 0
	v_fmac_f32_e32 v124, 0x3e0293ee, v0
	v_fmac_f32_e32 v125, 0x3e0293ee, v1
	v_max3_f32 v0, v124, s8, v125
	v_fmac_f32_e32 v126, 0x3e0293ee, v2
	v_fmac_f32_e32 v127, 0x3e0293ee, v3
	v_max3_f32 v0, v0, v126, v127
	v_fmac_f32_e32 v118, 0x3e0293ee, v4
	v_fmac_f32_e32 v119, 0x3e0293ee, v5
	v_max3_f32 v0, v0, v118, v119
	v_fmac_f32_e32 v120, 0x3e0293ee, v6
	v_fmac_f32_e32 v121, 0x3e0293ee, v7
	v_max3_f32 v0, v0, v120, v121
	v_fmac_f32_e32 v128, 0x3e0293ee, v8
	v_fmac_f32_e32 v129, 0x3e0293ee, v9
	v_max3_f32 v0, v0, v128, v129
	v_fmac_f32_e32 v123, 0x3e0293ee, v10
	v_fmac_f32_e32 v122, 0x3e0293ee, v11
	v_max3_f32 v0, v0, v123, v122
	v_fmac_f32_e32 v114, 0x3e0293ee, v12
	v_fmac_f32_e32 v115, 0x3e0293ee, v13
	v_max3_f32 v0, v0, v114, v115
	v_fmac_f32_e32 v116, 0x3e0293ee, v14
	v_fmac_f32_e32 v117, 0x3e0293ee, v15
	v_max3_f32 v0, v0, v116, v117
	v_mov_b32_e32 v1, v0
	v_mov_b32_e32 v2, v0
	v_and_b32_e32 v3, 32, v89
	s_nop 0
	v_permlane32_swap_b32_e32 v1, v2
	v_cmp_eq_u32_e32 vcc, 0, v3
	v_readlane_b32 s8, v252, 8
	s_nop 0
	v_cndmask_b32_e32 v1, v1, v2, vcc
	v_max_f32_e32 v1, v1, v1
	v_max_f32_e32 v0, v0, v1
	v_lshlrev_b32_e32 v1, 3, v130
	v_add_lshl_u32 v8, v1, s8, 2
	v_readlane_b32 s8, v255, 13
	s_nop 1
	v_add_u32_e32 v1, s8, v8
	ds_write_b32 v1, v0
	s_waitcnt lgkmcnt(0)
	s_barrier
	v_lshl_add_u32 v4, v130, 5, s8
	ds_read_b128 v[0:3], v4
	ds_read_b128 v[4:7], v4 offset:16
	v_add_u32_e32 v8, s9, v8
	v_readlane_b32 s8, v253, 21
	s_waitcnt lgkmcnt(1)
	v_max_f32_e32 v1, v1, v1
	v_max_f32_e32 v0, v0, v0
	v_max_f32_e32 v0, v0, v1
	v_max_f32_e32 v1, v3, v3
	v_max_f32_e32 v2, v2, v2
	v_max_f32_e32 v1, v2, v1
	s_waitcnt lgkmcnt(0)
	v_max_f32_e32 v2, v7, v7
	v_max_f32_e32 v3, v6, v6
	v_max_f32_e32 v2, v3, v2
	v_max3_f32 v2, v4, v5, v2
	v_max3_f32 v0, v0, v1, v2
	v_sub_f32_e32 v1, v124, v0
	v_sub_f32_e32 v2, v125, v0
	v_sub_f32_e32 v3, v126, v0
	v_sub_f32_e32 v4, v127, v0
	v_exp_f32_e32 v1, v1
	v_exp_f32_e32 v2, v2
	v_exp_f32_e32 v3, v3
	v_exp_f32_e32 v4, v4
	v_sub_f32_e32 v5, v118, v0
	v_sub_f32_e32 v6, v119, v0
	v_sub_f32_e32 v7, v120, v0
	v_sub_f32_e32 v9, v121, v0
	v_exp_f32_e32 v5, v5
	v_exp_f32_e32 v6, v6
	v_exp_f32_e32 v7, v7
	v_exp_f32_e32 v9, v9
	v_sub_f32_e32 v10, v128, v0
	v_sub_f32_e32 v11, v129, v0
	v_sub_f32_e32 v12, v123, v0
	v_sub_f32_e32 v13, v122, v0
	v_exp_f32_e32 v10, v10
	v_exp_f32_e32 v11, v11
	v_exp_f32_e32 v12, v12
	v_exp_f32_e32 v13, v13
	v_sub_f32_e32 v14, v114, v0
	v_sub_f32_e32 v15, v115, v0
	v_sub_f32_e32 v89, v116, v0
	v_sub_f32_e32 v0, v117, v0
	v_exp_f32_e32 v14, v14
	v_exp_f32_e32 v15, v15
	v_exp_f32_e32 v89, v89
	v_exp_f32_e32 v114, v0
	v_add_f32_e32 v0, v1, v2
	v_add_f32_e32 v115, v3, v4
	v_add_f32_e32 v0, v0, v115
	v_add_f32_e32 v115, v5, v6
	v_add_f32_e32 v116, v7, v9
	v_add_f32_e32 v115, v115, v116
	v_add_f32_e32 v0, v0, v115
	v_add_f32_e32 v115, v10, v11
	v_add_f32_e32 v116, v12, v13
	v_add_f32_e32 v115, v115, v116
	v_add_f32_e32 v116, v14, v15
	v_add_f32_e32 v117, v89, v114
	v_add_f32_e32 v116, v116, v117
	v_add_f32_e32 v115, v115, v116
	v_add_f32_e32 v0, v0, v115
	v_mov_b32_e32 v115, v0
	v_mov_b32_e32 v116, v0
	s_nop 1
	v_permlane32_swap_b32_e32 v115, v116
	v_cndmask_b32_e32 v115, v115, v116, vcc
	v_add_f32_e32 v0, v0, v115
	ds_write_b32 v8, v0
	v_add_u32_e32 v8, s8, v88
	v_cvt_pk_bf16_f32 v0, v1, v2
	v_cvt_pk_bf16_f32 v1, v3, v4
	v_cvt_pk_bf16_f32 v2, v5, v6
	v_cvt_pk_bf16_f32 v3, v7, v9
	ds_write_b128 v8, v[0:3]
	v_cvt_pk_bf16_f32 v0, v10, v11
	v_cvt_pk_bf16_f32 v1, v12, v13
	v_cvt_pk_bf16_f32 v2, v14, v15
	v_cvt_pk_bf16_f32 v3, v89, v114
	ds_write_b128 v8, v[0:3] offset:1024
	v_mov_b32_e32 v89, v90
	s_waitcnt lgkmcnt(0)
	s_barrier
	v_readlane_b32 s8, v253, 22
	v_and_b32_e32 v130, 31, v89
	v_lshl_add_u32 v4, v130, 5, s9
	ds_read_b128 v[0:3], v4
	ds_read_b128 v[4:7], v4 offset:16
	v_add_u32_e32 v131, s44, v89
	s_waitcnt lgkmcnt(1)
	v_add_f32_e32 v0, v0, v1
	v_add_f32_e32 v1, v2, v3
	v_add_f32_e32 v0, v0, v1
	s_waitcnt lgkmcnt(0)
	v_add_f32_e32 v1, v4, v5
	v_add_f32_e32 v2, v6, v7
	v_add_f32_e32 v1, v1, v2
	v_add_f32_e32 v0, v0, v1
	v_rcp_f32_e32 v0, v0
	v_lshl_add_u32 v1, v130, 2, s8
	s_cselect_b32 s8, s10, s16
	s_ashr_i32 s9, s8, 31
	ds_write_b32 v1, v0
	v_ashrrev_i32_e32 v0, 3, v89
	v_and_b32_e32 v88, -4, v0
	v_lshl_add_u32 v0, v89, 4, 0
	v_add_u32_e32 v129, 0x20000, v0
	ds_read_b128 v[0:3], v129
	ds_read_b64_tr_b16 v[4:5], v112
	ds_read_b64_tr_b16 v[6:7], v113
	s_lshl_b64 s[8:9], s[8:9], 10
	v_readlane_b32 s10, v253, 6
	s_add_u32 s10, s10, s8
	v_readlane_b32 s8, v253, 7
	s_addc_u32 s11, s8, s9
	v_readlane_b32 s8, v253, 8
	s_waitcnt lgkmcnt(0)
	v_mfma_f32_32x32x16_bf16 v[0:15], v[0:3], v[4:7], 0
	v_readlane_b32 s9, v253, 9
	s_add_u32 s8, s10, s8
	s_addc_u32 s9, s11, s9
	v_add_u32_e32 v128, 0x70, v88
	s_nop 1
	global_load_dword v121, v88, s[8:9]
	ds_read_b128 v[114:117], v129 offset:1024
	ds_read_b64_tr_b16 v[122:123], v112 offset:4096
	ds_read_b64_tr_b16 v[124:125], v113 offset:4096
	s_waitcnt lgkmcnt(0)
	v_mfma_f32_32x32x16_bf16 v[0:15], v[114:117], v[122:125], v[0:15]
	v_add_u32_e32 v114, 8, v88
	global_load_dword v123, v114, s[8:9]
	ds_read_b128 v[114:117], v129 offset:2048
	ds_read_b64_tr_b16 v[124:125], v112 offset:8192
	ds_read_b64_tr_b16 v[126:127], v113 offset:8192
	v_add_u32_e32 v122, 0x58, v88
	s_waitcnt lgkmcnt(0)
	v_mfma_f32_32x32x16_bf16 v[0:15], v[114:117], v[124:127], v[0:15]
	v_add_u32_e32 v114, 16, v88
	global_load_dword v116, v114, s[8:9]
	ds_read_b128 v[124:127], v129 offset:3072
	ds_read_b64_tr_b16 v[132:133], v112 offset:12288
	ds_read_b64_tr_b16 v[134:135], v113 offset:12288
	v_add_u32_e32 v114, 24, v88
	v_add_u32_e32 v115, 0x50, v88
	s_waitcnt lgkmcnt(0)
	v_mfma_f32_32x32x16_bf16 v[0:15], v[124:127], v[132:135], v[0:15]
	global_load_dword v124, v114, s[8:9]
	ds_read_b128 v[132:135], v129 offset:4096
	ds_read_b64_tr_b16 v[136:137], v112 offset:16384
	ds_read_b64_tr_b16 v[138:139], v113 offset:16384
	v_add_u32_e32 v114, 32, v88
	global_load_dword v119, v114, s[8:9]
	v_add_u32_e32 v114, 40, v88
	v_add_u32_e32 v126, 0x60, v88
	v_add_u32_e32 v127, 0x68, v88
	s_waitcnt lgkmcnt(0)
	v_mfma_f32_32x32x16_bf16 v[0:15], v[132:135], v[136:139], v[0:15]
	ds_read_b128 v[132:135], v129 offset:5120
	ds_read_b64_tr_b16 v[136:137], v112 offset:20480
	ds_read_b64_tr_b16 v[138:139], v113 offset:20480
	global_load_dword v120, v114, s[8:9]
	v_add_u32_e32 v114, 48, v88
	s_waitcnt lgkmcnt(0)
	v_mfma_f32_32x32x16_bf16 v[0:15], v[132:135], v[136:139], v[0:15]
	ds_read_b128 v[132:135], v129 offset:6144
	ds_read_b64_tr_b16 v[136:137], v112 offset:24576
	ds_read_b64_tr_b16 v[138:139], v113 offset:24576
	global_load_dword v117, v114, s[8:9]
	v_add_u32_e32 v114, 56, v88
	s_waitcnt lgkmcnt(0)
	v_mfma_f32_32x32x16_bf16 v[0:15], v[132:135], v[136:139], v[0:15]
	ds_read_b128 v[132:135], v129 offset:7168
	ds_read_b64_tr_b16 v[136:137], v112 offset:28672
	ds_read_b64_tr_b16 v[138:139], v113 offset:28672
	global_load_dword v125, v114, s[8:9]
	v_add_u32_e32 v114, 64, v88
	s_waitcnt lgkmcnt(0)
	v_mfma_f32_32x32x16_bf16 v[0:15], v[132:135], v[136:139], v[0:15]
	ds_read_b128 v[132:135], v129 offset:8192
	ds_read_b64_tr_b16 v[136:137], v112 offset:32768
	ds_read_b64_tr_b16 v[138:139], v113 offset:32768
	global_load_dword v118, v114, s[8:9]
	v_add_u32_e32 v114, 0x48, v88
	s_waitcnt lgkmcnt(0)
	v_mfma_f32_32x32x16_bf16 v[0:15], v[132:135], v[136:139], v[0:15]
	ds_read_b128 v[132:135], v129 offset:9216
	ds_read_b64_tr_b16 v[136:137], v112 offset:36864
	ds_read_b64_tr_b16 v[138:139], v113 offset:36864
	global_load_dword v114, v114, s[8:9]
	s_waitcnt lgkmcnt(0)
	v_mfma_f32_32x32x16_bf16 v[0:15], v[132:135], v[136:139], v[0:15]
	ds_read_b128 v[132:135], v129 offset:10240
	ds_read_b64_tr_b16 v[136:137], v112 offset:40960
	ds_read_b64_tr_b16 v[138:139], v113 offset:40960
	global_load_dword v115, v115, s[8:9]
	s_waitcnt lgkmcnt(0)
	v_mfma_f32_32x32x16_bf16 v[0:15], v[132:135], v[136:139], v[0:15]
	ds_read_b128 v[132:135], v129 offset:11264
	ds_read_b64_tr_b16 v[136:137], v112 offset:45056
	ds_read_b64_tr_b16 v[138:139], v113 offset:45056
	global_load_dword v122, v122, s[8:9]
	s_waitcnt lgkmcnt(0)
	v_mfma_f32_32x32x16_bf16 v[0:15], v[132:135], v[136:139], v[0:15]
	ds_read_b128 v[132:135], v129 offset:12288
	ds_read_b64_tr_b16 v[136:137], v112 offset:49152
	ds_read_b64_tr_b16 v[138:139], v113 offset:49152
	global_load_dword v126, v126, s[8:9]
	s_waitcnt lgkmcnt(0)
	v_mfma_f32_32x32x16_bf16 v[0:15], v[132:135], v[136:139], v[0:15]
	ds_read_b128 v[132:135], v129 offset:13312
	ds_read_b64_tr_b16 v[136:137], v112 offset:53248
	ds_read_b64_tr_b16 v[138:139], v113 offset:53248
	global_load_dword v127, v127, s[8:9]
	s_waitcnt lgkmcnt(0)
	v_mfma_f32_32x32x16_bf16 v[0:15], v[132:135], v[136:139], v[0:15]
	ds_read_b128 v[132:135], v129 offset:14336
	ds_read_b64_tr_b16 v[136:137], v112 offset:57344
	ds_read_b64_tr_b16 v[138:139], v113 offset:57344
	global_load_dword v128, v128, s[8:9]
	s_waitcnt lgkmcnt(0)
	v_mfma_f32_32x32x16_bf16 v[0:15], v[132:135], v[136:139], v[0:15]
	ds_read_b128 v[132:135], v129 offset:15360
	ds_read_b64_tr_b16 v[136:137], v112 offset:61440
	ds_read_b64_tr_b16 v[138:139], v113 offset:61440
	v_add_u32_e32 v129, 0x78, v88
	global_load_dword v129, v129, s[8:9]
	s_movk_i32 s8, 0x100
	v_cmp_gt_i32_e32 vcc, s8, v131
	s_waitcnt lgkmcnt(0)
	v_mfma_f32_32x32x16_bf16 v[0:15], v[132:135], v[136:139], v[0:15]
	s_and_saveexec_b64 s[8:9], vcc
	s_cbranch_execz .LBB0_803
	s_lshl_b64 s[12:13], s[44:45], 2
	s_add_u32 s10, s10, s12
	s_addc_u32 s11, s11, s13
	v_lshlrev_b32_e32 v89, 2, v89
	global_load_dword v91, v89, s[10:11]
	s_branch .LBB0_803

	.amdhsa_kernel _Z10fwd_kernel4Args
		.amdhsa_group_segment_fixed_size 0
		.amdhsa_private_segment_fixed_size 0
		.amdhsa_kernarg_size 432
		.amdhsa_user_sgpr_count 2
		.amdhsa_user_sgpr_dispatch_ptr 0
		.amdhsa_user_sgpr_queue_ptr 0
		.amdhsa_user_sgpr_kernarg_segment_ptr 1
		.amdhsa_user_sgpr_dispatch_id 0
		.amdhsa_user_sgpr_kernarg_preload_length 0
		.amdhsa_user_sgpr_kernarg_preload_offset 0
		.amdhsa_user_sgpr_private_segment_size 0
		.amdhsa_uses_dynamic_stack 0
		.amdhsa_enable_private_segment 0
		.amdhsa_system_sgpr_workgroup_id_x 1
		.amdhsa_system_sgpr_workgroup_id_y 0
		.amdhsa_system_sgpr_workgroup_id_z 0
		.amdhsa_system_sgpr_workgroup_info 0
		.amdhsa_system_vgpr_workitem_id 0
		.amdhsa_next_free_vgpr 256
		.amdhsa_next_free_sgpr 102
		.amdhsa_accum_offset 256
		.amdhsa_reserve_vcc 1
		.amdhsa_float_round_mode_32 0
		.amdhsa_float_round_mode_16_64 0
		.amdhsa_float_denorm_mode_32 3
		.amdhsa_float_denorm_mode_16_64 3
		.amdhsa_dx10_clamp 1
		.amdhsa_ieee_mode 1
		.amdhsa_fp16_overflow 0
		.amdhsa_tg_split 0
		.amdhsa_exception_fp_ieee_invalid_op 0
		.amdhsa_exception_fp_denorm_src 0
		.amdhsa_exception_fp_ieee_div_zero 0
		.amdhsa_exception_fp_ieee_overflow 0
		.amdhsa_exception_fp_ieee_underflow 0
		.amdhsa_exception_fp_ieee_inexact 0
		.amdhsa_exception_int_div_zero 0
	.end_amdhsa_kernel

amdhsa.kernels:
  - .agpr_count:     0
    .args:
      - .offset:         0
        .size:           176
        .value_kind:     by_value
      - .offset:         176
        .size:           4
        .value_kind:     hidden_block_count_x
      - .offset:         180
        .size:           4
        .value_kind:     hidden_block_count_y
      - .offset:         184
        .size:           4
        .value_kind:     hidden_block_count_z
      - .offset:         188
        .size:           2
        .value_kind:     hidden_group_size_x
      - .offset:         190
        .size:           2
        .value_kind:     hidden_group_size_y
      - .offset:         192
        .size:           2
        .value_kind:     hidden_group_size_z
      - .offset:         194
        .size:           2
        .value_kind:     hidden_remainder_x
      - .offset:         196
        .size:           2
        .value_kind:     hidden_remainder_y
      - .offset:         198
        .size:           2
        .value_kind:     hidden_remainder_z
      - .offset:         216
        .size:           8
        .value_kind:     hidden_global_offset_x
      - .offset:         224
        .size:           8
        .value_kind:     hidden_global_offset_y
      - .offset:         232
        .size:           8
        .value_kind:     hidden_global_offset_z
      - .offset:         240
        .size:           2
        .value_kind:     hidden_grid_dims
      - .offset:         296
        .size:           4
        .value_kind:     hidden_dynamic_lds_size
    .group_segment_fixed_size: 0
    .kernarg_segment_align: 8
    .kernarg_segment_size: 432
    .language:       OpenCL C
    .language_version:
      - 2
      - 0
    .max_flat_workgroup_size: 512
    .name:           _Z10fwd_kernel4Args
    .private_segment_fixed_size: 0
    .sgpr_count:     108
    .sgpr_spill_count: 232
    .symbol:         _Z10fwd_kernel4Args.kd
    .uniform_work_group_size: 1
    .uses_dynamic_stack: false
    .vgpr_count:     256
    .vgpr_spill_count: 0
    .wavefront_size: 64
